# stack5_det
# baseline (speedup 1.0000x reference)
.LBB0_4:
	s_or_b64 exec, exec, s[4:5]
	s_waitcnt lgkmcnt(0)
	s_barrier
	v_readfirstlane_b32 s8, v0
	s_lshr_b32 s8, s8, 6
	s_mov_b32 s9, 0
.Lsort_turn:
	s_cmp_lg_u32 s8, s9
	s_cbranch_scc1 .Lsort_skip
	ds_add_rtn_u32 v21, v14, v3 offset:256
	ds_add_rtn_u32 v22, v13, v3 offset:256
	ds_add_rtn_u32 v23, v11, v3 offset:256
	ds_add_rtn_u32 v24, v9, v3 offset:256
	s_waitcnt lgkmcnt(0)
.Lsort_skip:
	s_barrier
	s_add_u32 s9, s9, 1
	s_cmp_lt_u32 s9, 16
	s_cbranch_scc1 .Lsort_turn
	ds_read_b32 v15, v14
	s_load_dwordx2 s[4:5], s[0:1], 0x20
	s_waitcnt lgkmcnt(0)
	v_mov_b32_e32 v14, v21
	v_add_u32_e32 v14, v14, v15
	v_ashrrev_i32_e32 v16, 8, v14
	v_sub_u32_e32 v17, 15, v16
	v_cmp_gt_i32_e64 s[2:3], 8, v16
	v_lshrrev_b32_e32 v15, 6, v14
	s_nop 0
	v_cndmask_b32_e64 v16, v17, v16, s[2:3]
	v_cndmask_b32_e64 v17, 4, 0, s[2:3]
	v_mov_b32_e32 v20, 0x90
	v_lshrrev_b32_e32 v20, v16, v20
	v_and_b32_e32 v20, 1, v20
	v_mul_u32_u24_e32 v20, 3, v20
	v_xor_b32_e32 v16, v16, v20
	v_and_or_b32 v17, v15, 3, v17
	v_lshlrev_b32_e32 v15, 6, v16
	v_lshl_add_u32 v15, v17, 9, v15
	v_and_or_b32 v14, v14, 63, v15
	v_ashrrev_i32_e32 v15, 31, v14
	v_lshl_add_u64 v[14:15], v[14:15], 2, s[6:7]
	global_store_dword v[14:15], v0, off
	v_lshlrev_b32_e32 v14, 2, v17
	v_lshl_or_b32 v14, v16, 5, v14
	ds_max_i32 v14, v12 offset:768
	ds_read_b32 v12, v13
	s_waitcnt lgkmcnt(0)
	v_mov_b32_e32 v13, v22
	v_add_u32_e32 v12, v13, v12
	v_ashrrev_i32_e32 v14, 8, v12
	v_sub_u32_e32 v15, 15, v14
	v_cmp_gt_i32_e64 s[2:3], 8, v14
	v_lshrrev_b32_e32 v13, 6, v12
	s_nop 0
	v_cndmask_b32_e64 v14, v15, v14, s[2:3]
	v_cndmask_b32_e64 v15, 4, 0, s[2:3]
	v_mov_b32_e32 v20, 0x90
	v_lshrrev_b32_e32 v20, v14, v20
	v_and_b32_e32 v20, 1, v20
	v_mul_u32_u24_e32 v20, 3, v20
	v_xor_b32_e32 v14, v14, v20
	v_and_or_b32 v15, v13, 3, v15
	v_lshlrev_b32_e32 v13, 6, v14
	v_lshl_add_u32 v13, v15, 9, v13
	v_and_or_b32 v12, v12, 63, v13
	v_ashrrev_i32_e32 v13, 31, v12
	v_lshl_add_u64 v[12:13], v[12:13], 2, s[6:7]
	global_store_dword v[12:13], v8, off
	v_lshlrev_b32_e32 v8, 2, v15
	v_lshl_or_b32 v8, v14, 5, v8
	ds_max_i32 v8, v10 offset:768
	ds_read_b32 v8, v11
	s_waitcnt lgkmcnt(0)
	v_mov_b32_e32 v10, v23
	v_add_u32_e32 v8, v10, v8
	v_ashrrev_i32_e32 v11, 8, v8
	v_sub_u32_e32 v12, 15, v11
	v_cmp_gt_i32_e64 s[2:3], 8, v11
	v_lshrrev_b32_e32 v10, 6, v8
	s_nop 0
	v_cndmask_b32_e64 v12, v12, v11, s[2:3]
	v_cndmask_b32_e64 v11, 4, 0, s[2:3]
	v_mov_b32_e32 v20, 0x90
	v_lshrrev_b32_e32 v20, v12, v20
	v_and_b32_e32 v20, 1, v20
	v_mul_u32_u24_e32 v20, 3, v20
	v_xor_b32_e32 v12, v12, v20
	v_and_or_b32 v13, v10, 3, v11
	v_lshlrev_b32_e32 v10, 6, v12
	v_lshl_add_u32 v10, v13, 9, v10
	v_and_or_b32 v10, v8, 63, v10
	v_ashrrev_i32_e32 v11, 31, v10
	v_lshl_add_u64 v[10:11], v[10:11], 2, s[6:7]
	global_store_dword v[10:11], v6, off
	v_lshlrev_b32_e32 v6, 2, v13
	v_lshl_or_b32 v6, v12, 5, v6
	ds_max_i32 v6, v7 offset:768
	ds_read_b32 v6, v9
	s_waitcnt lgkmcnt(0)
	v_mov_b32_e32 v3, v24
	v_add_u32_e32 v3, v3, v6
	v_ashrrev_i32_e32 v7, 8, v3
	v_sub_u32_e32 v8, 15, v7
	v_cmp_gt_i32_e64 s[2:3], 8, v7
	v_lshrrev_b32_e32 v6, 6, v3
	s_nop 0
	v_cndmask_b32_e64 v8, v8, v7, s[2:3]
	v_cndmask_b32_e64 v7, 4, 0, s[2:3]
	v_mov_b32_e32 v20, 0x90
	v_lshrrev_b32_e32 v20, v8, v20
	v_and_b32_e32 v20, 1, v20
	v_mul_u32_u24_e32 v20, 3, v20
	v_xor_b32_e32 v8, v8, v20
	v_and_or_b32 v9, v6, 3, v7
	v_lshlrev_b32_e32 v6, 6, v8
	v_lshl_add_u32 v6, v9, 9, v6
	v_and_or_b32 v6, v3, 63, v6
	v_ashrrev_i32_e32 v7, 31, v6
	v_lshl_add_u64 v[6:7], v[6:7], 2, s[6:7]
	v_lshlrev_b32_e32 v3, 2, v9
	global_store_dword v[6:7], v4, off
	v_lshl_or_b32 v3, v8, 5, v3
	ds_max_i32 v3, v5 offset:768
	s_waitcnt lgkmcnt(0)
	s_barrier
	s_and_saveexec_b64 s[6:7], vcc
	s_cbranch_execz .LBB0_14
	v_and_b32_e32 v3, 60, v0
	v_add_u32_e32 v5, 1, v0
	v_sub_u32_e32 v6, v5, v3
	v_cmp_lt_u32_e64 s[2:3], 1, v6
	s_mov_b64 s[10:11], -1
	v_mov_b32_e32 v4, 0
	s_and_saveexec_b64 s[8:9], s[2:3]
	s_cbranch_execz .LBB0_9
	v_and_b32_e32 v5, 1, v5
	v_sub_u32_e32 v4, v6, v5
	v_mov_b32_e32 v6, 0x300
	v_lshl_or_b32 v7, v3, 2, v6
	v_mov_b32_e32 v6, 0
	s_mov_b64 s[10:11], 0
	v_mov_b32_e32 v9, v4
	v_mov_b32_e32 v8, 0

	.amdhsa_kernel _Z7k_sort2PKiPKfPiS3_S3_Pf
		.amdhsa_group_segment_fixed_size 1024
		.amdhsa_private_segment_fixed_size 0
		.amdhsa_kernarg_size 48
		.amdhsa_user_sgpr_count 2
		.amdhsa_user_sgpr_dispatch_ptr 0
		.amdhsa_user_sgpr_queue_ptr 0
		.amdhsa_user_sgpr_kernarg_segment_ptr 1
		.amdhsa_user_sgpr_dispatch_id 0
		.amdhsa_user_sgpr_kernarg_preload_length 0
		.amdhsa_user_sgpr_kernarg_preload_offset 0
		.amdhsa_user_sgpr_private_segment_size 0
		.amdhsa_uses_dynamic_stack 0
		.amdhsa_enable_private_segment 0
		.amdhsa_system_sgpr_workgroup_id_x 1
		.amdhsa_system_sgpr_workgroup_id_y 0
		.amdhsa_system_sgpr_workgroup_id_z 0
		.amdhsa_system_sgpr_workgroup_info 0
		.amdhsa_system_vgpr_workitem_id 0
		.amdhsa_next_free_vgpr 25
		.amdhsa_next_free_sgpr 12
		.amdhsa_accum_offset 28
		.amdhsa_reserve_vcc 1
		.amdhsa_float_round_mode_32 0
		.amdhsa_float_round_mode_16_64 0
		.amdhsa_float_denorm_mode_32 3
		.amdhsa_float_denorm_mode_16_64 3
		.amdhsa_dx10_clamp 1
		.amdhsa_ieee_mode 1
		.amdhsa_fp16_overflow 0
		.amdhsa_tg_split 0
		.amdhsa_exception_fp_ieee_invalid_op 0
		.amdhsa_exception_fp_denorm_src 0
		.amdhsa_exception_fp_ieee_div_zero 0
		.amdhsa_exception_fp_ieee_overflow 0
		.amdhsa_exception_fp_ieee_underflow 0
		.amdhsa_exception_fp_ieee_inexact 0
		.amdhsa_exception_int_div_zero 0
	.end_amdhsa_kernel

amdhsa.kernels:
  - .agpr_count:     0
    .args:
      - .actual_access:  read_only
        .address_space:  global
        .offset:         0
        .size:           8
        .value_kind:     global_buffer
      - .actual_access:  read_only
        .address_space:  global
        .offset:         8
        .size:           8
        .value_kind:     global_buffer
      - .actual_access:  write_only
        .address_space:  global
        .offset:         16
        .size:           8
        .value_kind:     global_buffer
      - .actual_access:  write_only
        .address_space:  global
        .offset:         24
        .size:           8
        .value_kind:     global_buffer
      - .actual_access:  write_only
        .address_space:  global
        .offset:         32
        .size:           8
        .value_kind:     global_buffer
      - .actual_access:  read_only
        .address_space:  global
        .offset:         40
        .size:           8
        .value_kind:     global_buffer
    .group_segment_fixed_size: 1024
    .kernarg_segment_align: 8
    .kernarg_segment_size: 48
    .language:       OpenCL C
    .language_version:
      - 2
      - 0
    .max_flat_workgroup_size: 1024
    .name:           _Z7k_sort2PKiPKfPiS3_S3_Pf
    .private_segment_fixed_size: 0
    .sgpr_count:     18
    .sgpr_spill_count: 0
    .symbol:         _Z7k_sort2PKiPKfPiS3_S3_Pf.kd
    .uniform_work_group_size: 1
    .uses_dynamic_stack: false
    .vgpr_count:     25
    .vgpr_spill_count: 0
    .wavefront_size: 64
  - .agpr_count:     0
    .args:
      - .actual_access:  read_only
        .address_space:  global
        .offset:         0
        .size:           8
        .value_kind:     global_buffer
      - .actual_access:  read_only
        .address_space:  global
        .offset:         8
        .size:           8
        .value_kind:     global_buffer
      - .actual_access:  read_only
        .address_space:  global
        .offset:         16
        .size:           8
        .value_kind:     global_buffer
      - .actual_access:  read_only
        .address_space:  global
        .offset:         24
        .size:           8
        .value_kind:     global_buffer
      - .actual_access:  read_only
        .address_space:  global
        .offset:         32
        .size:           8
        .value_kind:     global_buffer
      - .actual_access:  read_only
        .address_space:  global
        .offset:         40
        .size:           8
        .value_kind:     global_buffer
      - .address_space:  global
        .offset:         48
        .size:           8
        .value_kind:     global_buffer
      - .address_space:  global
        .offset:         56
        .size:           8
        .value_kind:     global_buffer
      - .offset:         64
        .size:           4
        .value_kind:     by_value
      - .offset:         68
        .size:           4
        .value_kind:     by_value
    .group_segment_fixed_size: 0
    .kernarg_segment_align: 8
    .kernarg_segment_size: 72
    .language:       OpenCL C
    .language_version:
      - 2
      - 0
    .max_flat_workgroup_size: 512
    .name:           _Z7k_spmm1PKiS0_PKfPK15HIP_vector_typeIjLj2EES0_S2_S2_Pfff
    .private_segment_fixed_size: 0
    .sgpr_count:     26
    .sgpr_spill_count: 0
    .symbol:         _Z7k_spmm1PKiS0_PKfPK15HIP_vector_typeIjLj2EES0_S2_S2_Pfff.kd
    .uniform_work_group_size: 1
    .uses_dynamic_stack: false
    .vgpr_count:     41
    .vgpr_spill_count: 0
    .wavefront_size: 64
  - .agpr_count:     0
    .args:
      - .address_space:  global
        .offset:         0
        .size:           8
        .value_kind:     global_buffer
      - .actual_access:  read_only
        .address_space:  global
        .offset:         8
        .size:           8
        .value_kind:     global_buffer
      - .actual_access:  read_only
        .address_space:  global
        .offset:         16
        .size:           8
        .value_kind:     global_buffer
      - .actual_access:  write_only
        .address_space:  global
        .offset:         24
        .size:           8
        .value_kind:     global_buffer
    .group_segment_fixed_size: 32768
    .kernarg_segment_align: 8
    .kernarg_segment_size: 32
    .language:       OpenCL C
    .language_version:
      - 2
      - 0
    .max_flat_workgroup_size: 512
    .name:           _Z7k_conv1PKfS0_S0_Pf
    .private_segment_fixed_size: 0
    .sgpr_count:     46
    .sgpr_spill_count: 0
    .symbol:         _Z7k_conv1PKfS0_S0_Pf.kd
    .uniform_work_group_size: 1
    .uses_dynamic_stack: false
    .vgpr_count:     107
    .vgpr_spill_count: 0
    .wavefront_size: 64
  - .agpr_count:     0
    .args:
      - .actual_access:  read_only
        .address_space:  global
        .offset:         0
        .size:           8
        .value_kind:     global_buffer
      - .actual_access:  read_only
        .address_space:  global
        .offset:         8
        .size:           8
        .value_kind:     global_buffer
      - .actual_access:  read_only
        .address_space:  global
        .offset:         16
        .size:           8
        .value_kind:     global_buffer
      - .address_space:  global
        .offset:         24
        .size:           8
        .value_kind:     global_buffer
      - .actual_access:  read_only
        .address_space:  global
        .offset:         32
        .size:           8
        .value_kind:     global_buffer
      - .actual_access:  read_only
        .address_space:  global
        .offset:         40
        .size:           8
        .value_kind:     global_buffer
      - .actual_access:  write_only
        .address_space:  global
        .offset:         48
        .size:           8
        .value_kind:     global_buffer
      - .actual_access:  write_only
        .address_space:  global
        .offset:         56
        .size:           8
        .value_kind:     global_buffer
      - .actual_access:  write_only
        .address_space:  global
        .offset:         64
        .size:           8
        .value_kind:     global_buffer
    .group_segment_fixed_size: 139392
    .kernarg_segment_align: 8
    .kernarg_segment_size: 72
    .language:       OpenCL C
    .language_version:
      - 2
      - 0
    .max_flat_workgroup_size: 512
    .name:           _Z6k_rec2PKiS0_S0_PK15HIP_vector_typeIjLj4EEPKfS6_PS2_PS1_IjLj2EEPf
    .private_segment_fixed_size: 0
    .sgpr_count:     75
    .sgpr_spill_count: 0
    .symbol:         _Z6k_rec2PKiS0_S0_PK15HIP_vector_typeIjLj4EEPKfS6_PS2_PS1_IjLj2EEPf.kd
    .uniform_work_group_size: 1
    .uses_dynamic_stack: false
    .vgpr_count:     246
    .vgpr_spill_count: 0
    .wavefront_size: 64
  - .agpr_count:     0
    .args:
      - .address_space:  global
        .offset:         0
        .size:           8
        .value_kind:     global_buffer
      - .address_space:  global
        .offset:         8
        .size:           8
        .value_kind:     global_buffer
      - .actual_access:  read_only
        .address_space:  global
        .offset:         16
        .size:           8
        .value_kind:     global_buffer
      - .actual_access:  read_only
        .address_space:  global
        .offset:         24
        .size:           8
        .value_kind:     global_buffer
      - .actual_access:  read_only
        .address_space:  global
        .offset:         32
        .size:           8
        .value_kind:     global_buffer
      - .actual_access:  read_only
        .address_space:  global
        .offset:         40
        .size:           8
        .value_kind:     global_buffer
      - .actual_access:  write_only
        .address_space:  global
        .offset:         48
        .size:           8
        .value_kind:     global_buffer
      - .actual_access:  write_only
        .address_space:  global
        .offset:         56
        .size:           8
        .value_kind:     global_buffer
    .group_segment_fixed_size: 127376
    .kernarg_segment_align: 8
    .kernarg_segment_size: 64
    .language:       OpenCL C
    .language_version:
      - 2
      - 0
    .max_flat_workgroup_size: 1024
    .name:           _Z7k_gemm2PK15HIP_vector_typeIjLj4EEPKS_IjLj2EEPKfS2_S2_S7_PtS8_
    .private_segment_fixed_size: 0
    .sgpr_count:     26
    .sgpr_spill_count: 0
    .symbol:         _Z7k_gemm2PK15HIP_vector_typeIjLj4EEPKS_IjLj2EEPKfS2_S2_S7_PtS8_.kd
    .uniform_work_group_size: 1
    .uses_dynamic_stack: false
    .vgpr_count:     115
    .vgpr_spill_count: 0
    .wavefront_size: 64
  - .agpr_count:     32
    .args:
      - .address_space:  global
        .offset:         0
        .size:           8
        .value_kind:     global_buffer
      - .address_space:  global
        .offset:         8
        .size:           8
        .value_kind:     global_buffer
      - .address_space:  global
        .offset:         16
        .size:           8
        .value_kind:     global_buffer
      - .actual_access:  write_only
        .address_space:  global
        .offset:         24
        .size:           8
        .value_kind:     global_buffer
    .group_segment_fixed_size: 65536
    .kernarg_segment_align: 8
    .kernarg_segment_size: 32
    .language:       OpenCL C
    .language_version:
      - 2
      - 0
    .max_flat_workgroup_size: 256
    .name:           _Z5k_fc1PKtS0_PKfPf
    .private_segment_fixed_size: 0
    .sgpr_count:     49
    .sgpr_spill_count: 0
    .symbol:         _Z5k_fc1PKtS0_PKfPf.kd
    .uniform_work_group_size: 1
    .uses_dynamic_stack: false
    .vgpr_count:     172
    .vgpr_spill_count: 0
    .wavefront_size: 64
  - .agpr_count:     0
    .args:
      - .actual_access:  read_only
        .address_space:  global
        .offset:         0
        .size:           8
        .value_kind:     global_buffer
      - .actual_access:  read_only
        .address_space:  global
        .offset:         8
        .size:           8
        .value_kind:     global_buffer
      - .actual_access:  read_only
        .address_space:  global
        .offset:         16
        .size:           8
        .value_kind:     global_buffer
      - .actual_access:  read_only
        .address_space:  global
        .offset:         24
        .size:           8
        .value_kind:     global_buffer
      - .actual_access:  write_only
        .address_space:  global
        .offset:         32
        .size:           8
        .value_kind:     global_buffer
    .group_segment_fixed_size: 2048
    .kernarg_segment_align: 8
    .kernarg_segment_size: 40
    .language:       OpenCL C
    .language_version:
      - 2
      - 0
    .max_flat_workgroup_size: 512
    .name:           _Z5k_fc2PKfS0_S0_S0_Pf
    .private_segment_fixed_size: 0
    .sgpr_count:     18
    .sgpr_spill_count: 0
    .symbol:         _Z5k_fc2PKfS0_S0_S0_Pf.kd
    .uniform_work_group_size: 1
    .uses_dynamic_stack: false
    .vgpr_count:     96
    .vgpr_spill_count: 0
    .wavefront_size: 64
  - .agpr_count:     0
    .args:
      - .actual_access:  read_only
        .address_space:  global
        .offset:         0
        .size:           8
        .value_kind:     global_buffer
      - .actual_access:  read_only
        .address_space:  global
        .offset:         8
        .size:           8
        .value_kind:     global_buffer
      - .actual_access:  read_only
        .address_space:  global
        .offset:         16
        .size:           8
        .value_kind:     global_buffer
      - .actual_access:  read_only
        .address_space:  global
        .offset:         24
        .size:           8
        .value_kind:     global_buffer
      - .actual_access:  write_only
        .address_space:  global
        .offset:         32
        .size:           8
        .value_kind:     global_buffer
      - .actual_access:  write_only
        .address_space:  global
        .offset:         40
        .size:           8
        .value_kind:     global_buffer
      - .actual_access:  write_only
        .address_space:  global
        .offset:         48
        .size:           8
        .value_kind:     global_buffer
      - .actual_access:  write_only
        .address_space:  global
        .offset:         56
        .size:           8
        .value_kind:     global_buffer
      - .actual_access:  write_only
        .address_space:  global
        .offset:         64
        .size:           8
        .value_kind:     global_buffer
    .group_segment_fixed_size: 16640
    .kernarg_segment_align: 8
    .kernarg_segment_size: 72
    .language:       OpenCL C
    .language_version:
      - 2
      - 0
    .max_flat_workgroup_size: 256
    .name:           _Z7k_prepAPKiS0_PKfS2_PiS3_PtS4_Pf
    .private_segment_fixed_size: 0
    .sgpr_count:     20
    .sgpr_spill_count: 0
    .symbol:         _Z7k_prepAPKiS0_PKfS2_PiS3_PtS4_Pf.kd
    .uniform_work_group_size: 1
    .uses_dynamic_stack: false
    .vgpr_count:     24
    .vgpr_spill_count: 0
    .wavefront_size: 64
  - .agpr_count:     0
    .args:
      - .actual_access:  read_only
        .address_space:  global
        .offset:         0
        .size:           8
        .value_kind:     global_buffer
      - .actual_access:  read_only
        .address_space:  global
        .offset:         8
        .size:           8
        .value_kind:     global_buffer
      - .actual_access:  read_only
        .address_space:  global
        .offset:         16
        .size:           8
        .value_kind:     global_buffer
      - .actual_access:  write_only
        .address_space:  global
        .offset:         24
        .size:           8
        .value_kind:     global_buffer
      - .actual_access:  write_only
        .address_space:  global
        .offset:         32
        .size:           8
        .value_kind:     global_buffer
      - .actual_access:  read_only
        .address_space:  global
        .offset:         40
        .size:           8
        .value_kind:     global_buffer
      - .actual_access:  read_only
        .address_space:  global
        .offset:         48
        .size:           8
        .value_kind:     global_buffer
      - .actual_access:  read_only
        .address_space:  global
        .offset:         56
        .size:           8
        .value_kind:     global_buffer
      - .actual_access:  read_only
        .address_space:  global
        .offset:         64
        .size:           8
        .value_kind:     global_buffer
      - .actual_access:  read_only
        .address_space:  global
        .offset:         72
        .size:           8
        .value_kind:     global_buffer
      - .actual_access:  read_only
        .address_space:  global
        .offset:         80
        .size:           8
        .value_kind:     global_buffer
      - .actual_access:  read_only
        .address_space:  global
        .offset:         88
        .size:           8
        .value_kind:     global_buffer
      - .actual_access:  write_only
        .address_space:  global
        .offset:         96
        .size:           8
        .value_kind:     global_buffer
    .group_segment_fixed_size: 0
    .kernarg_segment_align: 8
    .kernarg_segment_size: 104
    .language:       OpenCL C
    .language_version:
      - 2
      - 0
    .max_flat_workgroup_size: 256
    .name:           _Z7k_prepBPKiS0_PKfP15HIP_vector_typeIjLj2EEPiS0_S0_S2_S0_S0_S0_S2_Pj
    .private_segment_fixed_size: 0
    .sgpr_count:     21
    .sgpr_spill_count: 0
    .symbol:         _Z7k_prepBPKiS0_PKfP15HIP_vector_typeIjLj2EEPiS0_S0_S2_S0_S0_S0_S2_Pj.kd
    .uniform_work_group_size: 1
    .uses_dynamic_stack: false
    .vgpr_count:     14
    .vgpr_spill_count: 0
    .wavefront_size: 64
